# P7 epilogue: 32-bit store offsets on the scalar base (1 VALU instead of 4 64-bit ops per store), dead zero-inits of fully written fp8 dwords dropped (P7, P6)
# baseline (speedup 1.0000x reference)
; __device__ __forceinline__ unsigned pk4_fp8(float a, float b, float c, float d) { int r = __builtin_amdgcn_cvt_pk_fp8_f32(a, b, 0, false); r = __builtin_amdgcn_cvt_pk_fp8_f32(c, d, r, true); return (unsigned)r; }
;     __device__ __forceinline__ void operator()(const f32x4 (&acc)[2][2][4][2], const Unit& u, int wr, int wc, int fr, int fq) const {
;         const int row0 = u.pm * BM + wr * 64 + fr, col0 = (u.pn & 3) * 128 + wc * 32 + 8 * fq;
; #pragma unroll
;         for (int ai = 0; ai < 2; ++ai)
; #pragma unroll
;             for (int m = 0; m < 4; ++m) { float r[8];
; #pragma unroll
;                 for (int n = 0; n < 2; ++n)
; #pragma unroll
;                     for (int e = 0; e < 4; ++e) { const float g = acc[ai][0][m][n][e], up = acc[ai][1][m][n][e]; r[4 * n + e] = g * __builtin_amdgcn_rcpf(1.0f + __builtin_amdgcn_exp2f(-g * LOG2E)) * up * (float)(1 << ASHIFT); }
;                 v2u w; w.x = pk4_fp8(r[0], r[1], r[2], r[3]); w.y = pk4_fp8(r[4], r[5], r[6], r[7]);
;                 *(v2u*)(O + (size_t)(row0 + ai * HALF + m * 16) * EH + col0) = w; }
;     }
.LBB0_751:
	s_mov_b32 s98, 0xbfb8aa3b
	s_mov_b32 s100, 0x41800000
	s_nop 15
	s_nop 15
	v_lshl_add_u32 v4, s88, 8, v203
	s_lshl_b32 s6, s89, 7
	s_and_b32 s6, s6, 0x180
	v_ashrrev_i32_e32 v5, 31, v4
	v_add_u32_e32 v2, s6, v205
	v_lshlrev_b64 v[0:1], 9, v[4:5]
	v_ashrrev_i32_e32 v3, 31, v2
	v_lshl_add_u64 v[0:1], s[24:25], 0, v[0:1]
	v_lshl_add_u64 v[0:1], v[0:1], 0, v[2:3]
	v_pk_mul_f32 v[228:229], v[192:193], s[98:99] op_sel_hi:[1,0]
	v_pk_mul_f32 v[230:231], v[194:195], s[98:99] op_sel_hi:[1,0]
	v_pk_mul_f32 v[232:233], v[184:185], s[98:99] op_sel_hi:[1,0]
	v_pk_mul_f32 v[234:235], v[186:187], s[98:99] op_sel_hi:[1,0]
	v_exp_f32_e32 v228, v228
	v_exp_f32_e32 v229, v229
	v_exp_f32_e32 v230, v230
	v_exp_f32_e32 v231, v231
	v_exp_f32_e32 v232, v232
	v_exp_f32_e32 v233, v233
	v_exp_f32_e32 v234, v234
	v_exp_f32_e32 v235, v235
	v_pk_add_f32 v[228:229], v[228:229], 1.0 op_sel_hi:[1,0]
	v_pk_add_f32 v[230:231], v[230:231], 1.0 op_sel_hi:[1,0]
	v_pk_add_f32 v[232:233], v[232:233], 1.0 op_sel_hi:[1,0]
	v_pk_add_f32 v[234:235], v[234:235], 1.0 op_sel_hi:[1,0]
	v_rcp_f32_e32 v228, v228
	v_rcp_f32_e32 v229, v229
	v_rcp_f32_e32 v230, v230
	v_rcp_f32_e32 v231, v231
	v_rcp_f32_e32 v232, v232
	v_rcp_f32_e32 v233, v233
	v_rcp_f32_e32 v234, v234
	v_rcp_f32_e32 v235, v235
	v_pk_mul_f32 v[228:229], v[192:193], v[228:229]
	v_pk_mul_f32 v[230:231], v[194:195], v[230:231]
	v_pk_mul_f32 v[232:233], v[184:185], v[232:233]
	v_pk_mul_f32 v[234:235], v[186:187], v[234:235]
	v_pk_mul_f32 v[228:229], v[188:189], v[228:229]
	v_pk_mul_f32 v[230:231], v[190:191], v[230:231]
	v_pk_mul_f32 v[232:233], v[180:181], v[232:233]
	v_pk_mul_f32 v[234:235], v[182:183], v[234:235]
	v_pk_mul_f32 v[228:229], s[100:101], v[228:229] op_sel_hi:[0,1]
	v_pk_mul_f32 v[230:231], s[100:101], v[230:231] op_sel_hi:[0,1]
	v_pk_mul_f32 v[232:233], s[100:101], v[232:233] op_sel_hi:[0,1]
	v_pk_mul_f32 v[234:235], s[100:101], v[234:235] op_sel_hi:[0,1]
	v_cvt_pk_fp8_f32 v244, v228, v229
	v_cvt_pk_fp8_f32 v245, v232, v233
	v_cvt_pk_fp8_f32 v244, v230, v231 op_sel:[0,0,1]
	v_cvt_pk_fp8_f32 v245, v234, v235 op_sel:[0,0,1]
	s_nop 0
	global_store_dwordx2 v[0:1], v[244:245], off
	v_or_b32_e32 v8, 16, v4
	v_ashrrev_i32_e32 v9, 31, v8
	v_lshlrev_b64 v[8:9], 9, v[8:9]
	v_lshl_add_u64 v[8:9], s[24:25], 0, v[8:9]
	v_lshl_add_u64 v[8:9], v[8:9], 0, v[2:3]
	v_pk_mul_f32 v[228:229], v[176:177], s[98:99] op_sel_hi:[1,0]
	v_pk_mul_f32 v[230:231], v[178:179], s[98:99] op_sel_hi:[1,0]
	v_pk_mul_f32 v[232:233], v[168:169], s[98:99] op_sel_hi:[1,0]
	v_pk_mul_f32 v[234:235], v[170:171], s[98:99] op_sel_hi:[1,0]
	v_exp_f32_e32 v228, v228
	v_exp_f32_e32 v229, v229
	v_exp_f32_e32 v230, v230
	v_exp_f32_e32 v231, v231
	v_exp_f32_e32 v232, v232
	v_exp_f32_e32 v233, v233
	v_exp_f32_e32 v234, v234
	v_exp_f32_e32 v235, v235
	v_pk_add_f32 v[228:229], v[228:229], 1.0 op_sel_hi:[1,0]
	v_pk_add_f32 v[230:231], v[230:231], 1.0 op_sel_hi:[1,0]
	v_pk_add_f32 v[232:233], v[232:233], 1.0 op_sel_hi:[1,0]
	v_pk_add_f32 v[234:235], v[234:235], 1.0 op_sel_hi:[1,0]
	v_rcp_f32_e32 v228, v228
	v_rcp_f32_e32 v229, v229
	v_rcp_f32_e32 v230, v230
	v_rcp_f32_e32 v231, v231
	v_rcp_f32_e32 v232, v232
	v_rcp_f32_e32 v233, v233
	v_rcp_f32_e32 v234, v234
	v_rcp_f32_e32 v235, v235
	v_pk_mul_f32 v[228:229], v[176:177], v[228:229]
	v_pk_mul_f32 v[230:231], v[178:179], v[230:231]
	v_pk_mul_f32 v[232:233], v[168:169], v[232:233]
	v_pk_mul_f32 v[234:235], v[170:171], v[234:235]
	v_pk_mul_f32 v[228:229], v[172:173], v[228:229]
	v_pk_mul_f32 v[230:231], v[174:175], v[230:231]
	v_pk_mul_f32 v[232:233], v[164:165], v[232:233]
	v_pk_mul_f32 v[234:235], v[166:167], v[234:235]
	v_pk_mul_f32 v[228:229], s[100:101], v[228:229] op_sel_hi:[0,1]
	v_pk_mul_f32 v[230:231], s[100:101], v[230:231] op_sel_hi:[0,1]
	v_pk_mul_f32 v[232:233], s[100:101], v[232:233] op_sel_hi:[0,1]
	v_pk_mul_f32 v[234:235], s[100:101], v[234:235] op_sel_hi:[0,1]
	v_cvt_pk_fp8_f32 v244, v228, v229
	v_cvt_pk_fp8_f32 v245, v232, v233
	v_cvt_pk_fp8_f32 v244, v230, v231 op_sel:[0,0,1]
	v_cvt_pk_fp8_f32 v245, v234, v235 op_sel:[0,0,1]
	s_nop 0
	global_store_dwordx2 v[8:9], v[244:245], off
	v_or_b32_e32 v8, 32, v4
	v_ashrrev_i32_e32 v9, 31, v8
	v_lshlrev_b64 v[8:9], 9, v[8:9]
	v_lshl_add_u64 v[8:9], s[24:25], 0, v[8:9]
	v_lshl_add_u64 v[8:9], v[8:9], 0, v[2:3]
	v_pk_mul_f32 v[228:229], v[160:161], s[98:99] op_sel_hi:[1,0]
	v_pk_mul_f32 v[230:231], v[162:163], s[98:99] op_sel_hi:[1,0]
	v_pk_mul_f32 v[232:233], v[152:153], s[98:99] op_sel_hi:[1,0]
	v_pk_mul_f32 v[234:235], v[154:155], s[98:99] op_sel_hi:[1,0]
	v_exp_f32_e32 v228, v228
	v_exp_f32_e32 v229, v229
	v_exp_f32_e32 v230, v230
	v_exp_f32_e32 v231, v231
	v_exp_f32_e32 v232, v232
	v_exp_f32_e32 v233, v233
	v_exp_f32_e32 v234, v234
	v_exp_f32_e32 v235, v235
	v_pk_add_f32 v[228:229], v[228:229], 1.0 op_sel_hi:[1,0]
	v_pk_add_f32 v[230:231], v[230:231], 1.0 op_sel_hi:[1,0]
	v_pk_add_f32 v[232:233], v[232:233], 1.0 op_sel_hi:[1,0]
	v_pk_add_f32 v[234:235], v[234:235], 1.0 op_sel_hi:[1,0]
	v_rcp_f32_e32 v228, v228
	v_rcp_f32_e32 v229, v229
	v_rcp_f32_e32 v230, v230
	v_rcp_f32_e32 v231, v231
	v_rcp_f32_e32 v232, v232
	v_rcp_f32_e32 v233, v233
	v_rcp_f32_e32 v234, v234
	v_rcp_f32_e32 v235, v235
	v_pk_mul_f32 v[228:229], v[160:161], v[228:229]
	v_pk_mul_f32 v[230:231], v[162:163], v[230:231]
	v_pk_mul_f32 v[232:233], v[152:153], v[232:233]
	v_pk_mul_f32 v[234:235], v[154:155], v[234:235]
	v_pk_mul_f32 v[228:229], v[156:157], v[228:229]
	v_pk_mul_f32 v[230:231], v[158:159], v[230:231]
	v_pk_mul_f32 v[232:233], v[148:149], v[232:233]
	v_pk_mul_f32 v[234:235], v[150:151], v[234:235]
	v_pk_mul_f32 v[228:229], s[100:101], v[228:229] op_sel_hi:[0,1]
; __device__ __forceinline__ unsigned pk4_fp8(float a, float b, float c, float d) { int r = __builtin_amdgcn_cvt_pk_fp8_f32(a, b, 0, false); r = __builtin_amdgcn_cvt_pk_fp8_f32(c, d, r, true); return (unsigned)r; }
;     __device__ __forceinline__ void operator()(const f32x4 (&acc)[2][2][4][2], const Unit& u, int wr, int wc, int fr, int fq) const {
;         const int row0 = u.pm * BM + wr * 64 + fr, col0 = (u.pn & 3) * 128 + wc * 32 + 8 * fq;
; #pragma unroll
;         for (int ai = 0; ai < 2; ++ai)
; #pragma unroll
;             for (int m = 0; m < 4; ++m) { float r[8];
; #pragma unroll
;                 for (int n = 0; n < 2; ++n)
; #pragma unroll
;                     for (int e = 0; e < 4; ++e) { const float g = acc[ai][0][m][n][e], up = acc[ai][1][m][n][e]; r[4 * n + e] = g * __builtin_amdgcn_rcpf(1.0f + __builtin_amdgcn_exp2f(-g * LOG2E)) * up * (float)(1 << ASHIFT); }
;                 v2u w; w.x = pk4_fp8(r[0], r[1], r[2], r[3]); w.y = pk4_fp8(r[4], r[5], r[6], r[7]);
;                 *(v2u*)(O + (size_t)(row0 + ai * HALF + m * 16) * EH + col0) = w; }
;     }
	v_pk_mul_f32 v[230:231], s[100:101], v[230:231] op_sel_hi:[0,1]
	v_pk_mul_f32 v[232:233], s[100:101], v[232:233] op_sel_hi:[0,1]
	v_pk_mul_f32 v[234:235], s[100:101], v[234:235] op_sel_hi:[0,1]
	v_cvt_pk_fp8_f32 v244, v228, v229
	v_cvt_pk_fp8_f32 v245, v232, v233
	v_cvt_pk_fp8_f32 v244, v230, v231 op_sel:[0,0,1]
	v_cvt_pk_fp8_f32 v245, v234, v235 op_sel:[0,0,1]
	s_nop 0
	global_store_dwordx2 v[8:9], v[244:245], off
	v_or_b32_e32 v4, 48, v4
	v_ashrrev_i32_e32 v5, 31, v4
	v_lshlrev_b64 v[4:5], 9, v[4:5]
	v_lshl_add_u64 v[4:5], s[24:25], 0, v[4:5]
	v_lshl_add_u64 v[2:3], v[4:5], 0, v[2:3]
	v_pk_mul_f32 v[228:229], v[144:145], s[98:99] op_sel_hi:[1,0]
	v_pk_mul_f32 v[230:231], v[146:147], s[98:99] op_sel_hi:[1,0]
	v_pk_mul_f32 v[232:233], v[136:137], s[98:99] op_sel_hi:[1,0]
	v_pk_mul_f32 v[234:235], v[138:139], s[98:99] op_sel_hi:[1,0]
	v_exp_f32_e32 v228, v228
	v_exp_f32_e32 v229, v229
	v_exp_f32_e32 v230, v230
	v_exp_f32_e32 v231, v231
	v_exp_f32_e32 v232, v232
	v_exp_f32_e32 v233, v233
	v_exp_f32_e32 v234, v234
	v_exp_f32_e32 v235, v235
	v_pk_add_f32 v[228:229], v[228:229], 1.0 op_sel_hi:[1,0]
	v_pk_add_f32 v[230:231], v[230:231], 1.0 op_sel_hi:[1,0]
	v_pk_add_f32 v[232:233], v[232:233], 1.0 op_sel_hi:[1,0]
	v_pk_add_f32 v[234:235], v[234:235], 1.0 op_sel_hi:[1,0]
	v_rcp_f32_e32 v228, v228
	v_rcp_f32_e32 v229, v229
	v_rcp_f32_e32 v230, v230
	v_rcp_f32_e32 v231, v231
	v_rcp_f32_e32 v232, v232
	v_rcp_f32_e32 v233, v233
	v_rcp_f32_e32 v234, v234
	v_rcp_f32_e32 v235, v235
	v_pk_mul_f32 v[228:229], v[144:145], v[228:229]
	v_pk_mul_f32 v[230:231], v[146:147], v[230:231]
	v_pk_mul_f32 v[232:233], v[136:137], v[232:233]
	v_pk_mul_f32 v[234:235], v[138:139], v[234:235]
	v_pk_mul_f32 v[228:229], v[140:141], v[228:229]
	v_pk_mul_f32 v[230:231], v[142:143], v[230:231]
	v_pk_mul_f32 v[232:233], v[132:133], v[232:233]
	v_pk_mul_f32 v[234:235], v[134:135], v[234:235]
	v_pk_mul_f32 v[228:229], s[100:101], v[228:229] op_sel_hi:[0,1]
	v_pk_mul_f32 v[230:231], s[100:101], v[230:231] op_sel_hi:[0,1]
	v_pk_mul_f32 v[232:233], s[100:101], v[232:233] op_sel_hi:[0,1]
	v_pk_mul_f32 v[234:235], s[100:101], v[234:235] op_sel_hi:[0,1]
	v_cvt_pk_fp8_f32 v244, v228, v229
	v_cvt_pk_fp8_f32 v245, v232, v233
	v_cvt_pk_fp8_f32 v244, v230, v231 op_sel:[0,0,1]
	v_cvt_pk_fp8_f32 v245, v234, v235 op_sel:[0,0,1]
	s_nop 0
	global_store_dwordx2 v[2:3], v[244:245], off
	v_add_co_u32_e32 v4, vcc, s50, v0
	s_nop 0
	v_addc_co_u32_e32 v5, vcc, 0, v1, vcc
	v_pk_mul_f32 v[228:229], v[128:129], s[98:99] op_sel_hi:[1,0]
	v_pk_mul_f32 v[230:231], v[130:131], s[98:99] op_sel_hi:[1,0]
	v_pk_mul_f32 v[232:233], v[120:121], s[98:99] op_sel_hi:[1,0]
	v_pk_mul_f32 v[234:235], v[122:123], s[98:99] op_sel_hi:[1,0]
	v_exp_f32_e32 v228, v228
	v_exp_f32_e32 v229, v229
	v_exp_f32_e32 v230, v230
	v_exp_f32_e32 v231, v231
	v_exp_f32_e32 v232, v232
	v_exp_f32_e32 v233, v233
	v_exp_f32_e32 v234, v234
	v_exp_f32_e32 v235, v235
	v_pk_add_f32 v[228:229], v[228:229], 1.0 op_sel_hi:[1,0]
	v_pk_add_f32 v[230:231], v[230:231], 1.0 op_sel_hi:[1,0]
	v_pk_add_f32 v[232:233], v[232:233], 1.0 op_sel_hi:[1,0]
	v_pk_add_f32 v[234:235], v[234:235], 1.0 op_sel_hi:[1,0]
	v_rcp_f32_e32 v228, v228
	v_rcp_f32_e32 v229, v229
	v_rcp_f32_e32 v230, v230
	v_rcp_f32_e32 v231, v231
	v_rcp_f32_e32 v232, v232
	v_rcp_f32_e32 v233, v233
	v_rcp_f32_e32 v234, v234
	v_rcp_f32_e32 v235, v235
	v_pk_mul_f32 v[228:229], v[128:129], v[228:229]
	v_pk_mul_f32 v[230:231], v[130:131], v[230:231]
	v_pk_mul_f32 v[232:233], v[120:121], v[232:233]
	v_pk_mul_f32 v[234:235], v[122:123], v[234:235]
	v_pk_mul_f32 v[228:229], v[124:125], v[228:229]
	v_pk_mul_f32 v[230:231], v[126:127], v[230:231]
	v_pk_mul_f32 v[232:233], v[116:117], v[232:233]
	v_pk_mul_f32 v[234:235], v[118:119], v[234:235]
	v_pk_mul_f32 v[228:229], s[100:101], v[228:229] op_sel_hi:[0,1]
	v_pk_mul_f32 v[230:231], s[100:101], v[230:231] op_sel_hi:[0,1]
	v_pk_mul_f32 v[232:233], s[100:101], v[232:233] op_sel_hi:[0,1]
	v_pk_mul_f32 v[234:235], s[100:101], v[234:235] op_sel_hi:[0,1]
	v_cvt_pk_fp8_f32 v244, v228, v229
	v_cvt_pk_fp8_f32 v245, v232, v233
	v_cvt_pk_fp8_f32 v244, v230, v231 op_sel:[0,0,1]
	v_cvt_pk_fp8_f32 v245, v234, v235 op_sel:[0,0,1]
	s_nop 0
	global_store_dwordx2 v[4:5], v[244:245], off
	v_add_co_u32_e32 v4, vcc, s52, v0
	s_nop 0
	v_addc_co_u32_e32 v5, vcc, 0, v1, vcc
	v_pk_mul_f32 v[228:229], v[112:113], s[98:99] op_sel_hi:[1,0]
	v_pk_mul_f32 v[230:231], v[114:115], s[98:99] op_sel_hi:[1,0]
	v_pk_mul_f32 v[232:233], v[104:105], s[98:99] op_sel_hi:[1,0]
	v_pk_mul_f32 v[234:235], v[106:107], s[98:99] op_sel_hi:[1,0]
	v_exp_f32_e32 v228, v228
	v_exp_f32_e32 v229, v229
	v_exp_f32_e32 v230, v230
	v_exp_f32_e32 v231, v231
	v_exp_f32_e32 v232, v232
	v_exp_f32_e32 v233, v233
	v_exp_f32_e32 v234, v234
	v_exp_f32_e32 v235, v235
	v_pk_add_f32 v[228:229], v[228:229], 1.0 op_sel_hi:[1,0]
	v_pk_add_f32 v[230:231], v[230:231], 1.0 op_sel_hi:[1,0]
	v_pk_add_f32 v[232:233], v[232:233], 1.0 op_sel_hi:[1,0]
; __device__ __forceinline__ unsigned pk4_fp8(float a, float b, float c, float d) { int r = __builtin_amdgcn_cvt_pk_fp8_f32(a, b, 0, false); r = __builtin_amdgcn_cvt_pk_fp8_f32(c, d, r, true); return (unsigned)r; }
;     __device__ __forceinline__ void operator()(const f32x4 (&acc)[2][2][4][2], const Unit& u, int wr, int wc, int fr, int fq) const {
;         const int row0 = u.pm * BM + wr * 64 + fr, col0 = (u.pn & 3) * 128 + wc * 32 + 8 * fq;
; #pragma unroll
;         for (int ai = 0; ai < 2; ++ai)
; #pragma unroll
;             for (int m = 0; m < 4; ++m) { float r[8];
; #pragma unroll
;                 for (int n = 0; n < 2; ++n)
; #pragma unroll
;                     for (int e = 0; e < 4; ++e) { const float g = acc[ai][0][m][n][e], up = acc[ai][1][m][n][e]; r[4 * n + e] = g * __builtin_amdgcn_rcpf(1.0f + __builtin_amdgcn_exp2f(-g * LOG2E)) * up * (float)(1 << ASHIFT); }
;                 v2u w; w.x = pk4_fp8(r[0], r[1], r[2], r[3]); w.y = pk4_fp8(r[4], r[5], r[6], r[7]);
;                 *(v2u*)(O + (size_t)(row0 + ai * HALF + m * 16) * EH + col0) = w; }
;     }
	v_pk_add_f32 v[234:235], v[234:235], 1.0 op_sel_hi:[1,0]
	v_rcp_f32_e32 v228, v228
	v_rcp_f32_e32 v229, v229
	v_rcp_f32_e32 v230, v230
	v_rcp_f32_e32 v231, v231
	v_rcp_f32_e32 v232, v232
	v_rcp_f32_e32 v233, v233
	v_rcp_f32_e32 v234, v234
	v_rcp_f32_e32 v235, v235
	v_pk_mul_f32 v[228:229], v[112:113], v[228:229]
	v_pk_mul_f32 v[230:231], v[114:115], v[230:231]
	v_pk_mul_f32 v[232:233], v[104:105], v[232:233]
	v_pk_mul_f32 v[234:235], v[106:107], v[234:235]
	v_pk_mul_f32 v[228:229], v[108:109], v[228:229]
	v_pk_mul_f32 v[230:231], v[110:111], v[230:231]
	v_pk_mul_f32 v[232:233], v[100:101], v[232:233]
	v_pk_mul_f32 v[234:235], v[102:103], v[234:235]
	v_pk_mul_f32 v[228:229], s[100:101], v[228:229] op_sel_hi:[0,1]
	v_pk_mul_f32 v[230:231], s[100:101], v[230:231] op_sel_hi:[0,1]
	v_pk_mul_f32 v[232:233], s[100:101], v[232:233] op_sel_hi:[0,1]
	v_pk_mul_f32 v[234:235], s[100:101], v[234:235] op_sel_hi:[0,1]
	v_cvt_pk_fp8_f32 v244, v228, v229
	v_cvt_pk_fp8_f32 v245, v232, v233
	v_cvt_pk_fp8_f32 v244, v230, v231 op_sel:[0,0,1]
	v_cvt_pk_fp8_f32 v245, v234, v235 op_sel:[0,0,1]
	s_nop 0
	global_store_dwordx2 v[4:5], v[244:245], off
	v_add_co_u32_e32 v4, vcc, s54, v0
	s_nop 0
	v_addc_co_u32_e32 v5, vcc, 0, v1, vcc
	v_pk_mul_f32 v[228:229], v[96:97], s[98:99] op_sel_hi:[1,0]
	v_pk_mul_f32 v[230:231], v[98:99], s[98:99] op_sel_hi:[1,0]
	v_pk_mul_f32 v[232:233], v[88:89], s[98:99] op_sel_hi:[1,0]
	v_pk_mul_f32 v[234:235], v[90:91], s[98:99] op_sel_hi:[1,0]
	v_exp_f32_e32 v228, v228
	v_exp_f32_e32 v229, v229
	v_exp_f32_e32 v230, v230
	v_exp_f32_e32 v231, v231
	v_exp_f32_e32 v232, v232
	v_exp_f32_e32 v233, v233
	v_exp_f32_e32 v234, v234
	v_exp_f32_e32 v235, v235
	v_pk_add_f32 v[228:229], v[228:229], 1.0 op_sel_hi:[1,0]
	v_pk_add_f32 v[230:231], v[230:231], 1.0 op_sel_hi:[1,0]
	v_pk_add_f32 v[232:233], v[232:233], 1.0 op_sel_hi:[1,0]
	v_pk_add_f32 v[234:235], v[234:235], 1.0 op_sel_hi:[1,0]
	v_rcp_f32_e32 v228, v228
	v_rcp_f32_e32 v229, v229
	v_rcp_f32_e32 v230, v230
	v_rcp_f32_e32 v231, v231
	v_rcp_f32_e32 v232, v232
	v_rcp_f32_e32 v233, v233
	v_rcp_f32_e32 v234, v234
	v_rcp_f32_e32 v235, v235
	v_pk_mul_f32 v[228:229], v[96:97], v[228:229]
	v_pk_mul_f32 v[230:231], v[98:99], v[230:231]
	v_pk_mul_f32 v[232:233], v[88:89], v[232:233]
	v_pk_mul_f32 v[234:235], v[90:91], v[234:235]
	v_pk_mul_f32 v[228:229], v[92:93], v[228:229]
	v_pk_mul_f32 v[230:231], v[94:95], v[230:231]
	v_pk_mul_f32 v[232:233], v[84:85], v[232:233]
	v_pk_mul_f32 v[234:235], v[86:87], v[234:235]
	v_pk_mul_f32 v[228:229], s[100:101], v[228:229] op_sel_hi:[0,1]
	v_pk_mul_f32 v[230:231], s[100:101], v[230:231] op_sel_hi:[0,1]
	v_pk_mul_f32 v[232:233], s[100:101], v[232:233] op_sel_hi:[0,1]
	v_pk_mul_f32 v[234:235], s[100:101], v[234:235] op_sel_hi:[0,1]
	v_cvt_pk_fp8_f32 v244, v228, v229
	v_cvt_pk_fp8_f32 v245, v232, v233
	v_cvt_pk_fp8_f32 v244, v230, v231 op_sel:[0,0,1]
	v_cvt_pk_fp8_f32 v245, v234, v235 op_sel:[0,0,1]
	s_nop 0
	global_store_dwordx2 v[4:5], v[244:245], off
	v_add_co_u32_e32 v0, vcc, 0x16000, v0
	s_nop 1
	v_addc_co_u32_e32 v1, vcc, 0, v1, vcc
	s_and_b64 vcc, exec, s[4:5]
	s_mov_b64 s[4:5], -1
	v_pk_mul_f32 v[228:229], v[80:81], s[98:99] op_sel_hi:[1,0]
	v_pk_mul_f32 v[230:231], v[82:83], s[98:99] op_sel_hi:[1,0]
	v_pk_mul_f32 v[232:233], v[72:73], s[98:99] op_sel_hi:[1,0]
	v_pk_mul_f32 v[234:235], v[74:75], s[98:99] op_sel_hi:[1,0]
	v_exp_f32_e32 v228, v228
	v_exp_f32_e32 v229, v229
	v_exp_f32_e32 v230, v230
	v_exp_f32_e32 v231, v231
	v_exp_f32_e32 v232, v232
	v_exp_f32_e32 v233, v233
	v_exp_f32_e32 v234, v234
	v_exp_f32_e32 v235, v235
	v_pk_add_f32 v[228:229], v[228:229], 1.0 op_sel_hi:[1,0]
	v_pk_add_f32 v[230:231], v[230:231], 1.0 op_sel_hi:[1,0]
	v_pk_add_f32 v[232:233], v[232:233], 1.0 op_sel_hi:[1,0]
	v_pk_add_f32 v[234:235], v[234:235], 1.0 op_sel_hi:[1,0]
	v_rcp_f32_e32 v228, v228
	v_rcp_f32_e32 v229, v229
	v_rcp_f32_e32 v230, v230
	v_rcp_f32_e32 v231, v231
	v_rcp_f32_e32 v232, v232
	v_rcp_f32_e32 v233, v233
	v_rcp_f32_e32 v234, v234
	v_rcp_f32_e32 v235, v235
	v_pk_mul_f32 v[228:229], v[80:81], v[228:229]
	v_pk_mul_f32 v[230:231], v[82:83], v[230:231]
	v_pk_mul_f32 v[232:233], v[72:73], v[232:233]
	v_pk_mul_f32 v[234:235], v[74:75], v[234:235]
	v_pk_mul_f32 v[228:229], v[76:77], v[228:229]
	v_pk_mul_f32 v[230:231], v[78:79], v[230:231]
	v_pk_mul_f32 v[232:233], v[68:69], v[232:233]
	v_pk_mul_f32 v[234:235], v[70:71], v[234:235]
	v_pk_mul_f32 v[228:229], s[100:101], v[228:229] op_sel_hi:[0,1]
	v_pk_mul_f32 v[230:231], s[100:101], v[230:231] op_sel_hi:[0,1]
	v_pk_mul_f32 v[232:233], s[100:101], v[232:233] op_sel_hi:[0,1]
	v_pk_mul_f32 v[234:235], s[100:101], v[234:235] op_sel_hi:[0,1]
	v_cvt_pk_fp8_f32 v244, v228, v229
	v_cvt_pk_fp8_f32 v245, v232, v233
	v_cvt_pk_fp8_f32 v244, v230, v231 op_sel:[0,0,1]
	v_cvt_pk_fp8_f32 v245, v234, v235 op_sel:[0,0,1]
	s_nop 0
	global_store_dwordx2 v[0:1], v[244:245], off
	s_cbranch_vccnz .LBB0_715
	s_andn2_b64 vcc, exec, s[22:23]
	s_cbranch_vccnz .LBB0_714
	s_barrier
	s_branch .LBB0_714

; __device__ __forceinline__ unsigned pk4_fp8(float a, float b, float c, float d) { int r = __builtin_amdgcn_cvt_pk_fp8_f32(a, b, 0, false); r = __builtin_amdgcn_cvt_pk_fp8_f32(c, d, r, true); return (unsigned)r; }
;     __device__ __forceinline__ void operator()(const f32x4 (&acc)[2][2][4][2], const Unit& u, int wr, int wc, int fr, int fq) const {
;     ...
;         for (int ai = 0; ai < 2; ++ai)
; #pragma unroll
;             for (int m = 0; m < 4; ++m) { unsigned char* rowp = O + (size_t)drow[ai][m] * D + col0;
;                 const f32x4 a0 = acc[ai][0][m][0] * ysc, a1 = acc[ai][0][m][1] * ysc, b0 = acc[ai][1][m][0] * ysc, b1 = acc[ai][1][m][1] * ysc;
;                 v4u w; w.x = pk4_fp8(a0[0], a0[1], a0[2], a0[3]); w.y = pk4_fp8(a1[0], a1[1], a1[2], a1[3]); w.z = pk4_fp8(b0[0], b0[1], b0[2], b0[3]); w.w = pk4_fp8(b1[0], b1[1], b1[2], b1[3]);
;                 *(v4u*)rowp = w; }
.LBB0_903:
	v_cvt_pk_fp8_f32 v18, v156, v157
	v_cvt_pk_fp8_f32 v19, v152, v153
	v_cvt_pk_fp8_f32 v20, v148, v149
	v_cvt_pk_fp8_f32 v21, v144, v145
	s_lshl_b32 s6, s73, 8
	s_and_b32 s6, s6, 0x700
	s_waitcnt vmcnt(0)
	v_cvt_pk_fp8_f32 v18, v158, v159 op_sel:[0,0,1]
	v_cvt_pk_fp8_f32 v19, v154, v155 op_sel:[0,0,1]
	v_cvt_pk_fp8_f32 v20, v150, v151 op_sel:[0,0,1]
	v_cvt_pk_fp8_f32 v21, v146, v147 op_sel:[0,0,1]
	v_add_u32_e32 v16, s6, v163
	v_lshl_add_u32 v11, v10, 11, v16
	global_store_dwordx4 v11, v[18:21], s[18:19]
	s_nop 1
	v_cvt_pk_fp8_f32 v18, v140, v141
	v_cvt_pk_fp8_f32 v19, v136, v137
	v_cvt_pk_fp8_f32 v20, v132, v133
	v_cvt_pk_fp8_f32 v21, v128, v129
	v_cvt_pk_fp8_f32 v18, v142, v143 op_sel:[0,0,1]
	v_cvt_pk_fp8_f32 v19, v138, v139 op_sel:[0,0,1]
	v_cvt_pk_fp8_f32 v20, v134, v135 op_sel:[0,0,1]
	v_cvt_pk_fp8_f32 v21, v130, v131 op_sel:[0,0,1]
	v_lshl_add_u32 v11, v14, 11, v16
	global_store_dwordx4 v11, v[18:21], s[18:19]
	s_nop 1
	v_cvt_pk_fp8_f32 v19, v120, v121
	v_cvt_pk_fp8_f32 v18, v124, v125
	v_cvt_pk_fp8_f32 v20, v116, v117
	v_cvt_pk_fp8_f32 v21, v112, v113
	v_cvt_pk_fp8_f32 v18, v126, v127 op_sel:[0,0,1]
	v_cvt_pk_fp8_f32 v19, v122, v123 op_sel:[0,0,1]
	v_cvt_pk_fp8_f32 v20, v118, v119 op_sel:[0,0,1]
	v_cvt_pk_fp8_f32 v21, v114, v115 op_sel:[0,0,1]
	v_lshl_add_u32 v11, v12, 11, v16
	global_store_dwordx4 v11, v[18:21], s[18:19]
	s_nop 1
	v_cvt_pk_fp8_f32 v10, v108, v109
	v_cvt_pk_fp8_f32 v11, v104, v105
	v_cvt_pk_fp8_f32 v12, v100, v101
	v_cvt_pk_fp8_f32 v13, v96, v97
	v_cvt_pk_fp8_f32 v10, v110, v111 op_sel:[0,0,1]
	v_cvt_pk_fp8_f32 v11, v106, v107 op_sel:[0,0,1]
	v_cvt_pk_fp8_f32 v12, v102, v103 op_sel:[0,0,1]
	v_cvt_pk_fp8_f32 v13, v98, v99 op_sel:[0,0,1]
	v_lshl_add_u32 v9, v8, 11, v16
	global_store_dwordx4 v9, v[10:13], s[18:19]
	s_nop 1
	v_cvt_pk_fp8_f32 v8, v92, v93
	v_cvt_pk_fp8_f32 v9, v88, v89
	v_cvt_pk_fp8_f32 v10, v84, v85
	v_cvt_pk_fp8_f32 v11, v80, v81
	v_cvt_pk_fp8_f32 v8, v94, v95 op_sel:[0,0,1]
	v_cvt_pk_fp8_f32 v9, v90, v91 op_sel:[0,0,1]
	v_cvt_pk_fp8_f32 v10, v86, v87 op_sel:[0,0,1]
	v_cvt_pk_fp8_f32 v11, v82, v83 op_sel:[0,0,1]
	v_lshl_add_u32 v7, v6, 11, v16
	global_store_dwordx4 v7, v[8:11], s[18:19]
	s_nop 1
	v_cvt_pk_fp8_f32 v6, v76, v77
	v_cvt_pk_fp8_f32 v7, v72, v73
	v_cvt_pk_fp8_f32 v8, v68, v69
	v_cvt_pk_fp8_f32 v9, v64, v65
	v_cvt_pk_fp8_f32 v6, v78, v79 op_sel:[0,0,1]
	v_cvt_pk_fp8_f32 v7, v74, v75 op_sel:[0,0,1]
	v_cvt_pk_fp8_f32 v8, v70, v71 op_sel:[0,0,1]
	v_cvt_pk_fp8_f32 v9, v66, v67 op_sel:[0,0,1]
	v_lshl_add_u32 v5, v4, 11, v16
	global_store_dwordx4 v5, v[6:9], s[18:19]
	s_nop 1
	v_cvt_pk_fp8_f32 v4, v60, v61
	v_cvt_pk_fp8_f32 v5, v56, v57
	v_cvt_pk_fp8_f32 v6, v52, v53
	v_cvt_pk_fp8_f32 v7, v48, v49
	v_cvt_pk_fp8_f32 v4, v62, v63 op_sel:[0,0,1]
	v_cvt_pk_fp8_f32 v5, v58, v59 op_sel:[0,0,1]
	v_cvt_pk_fp8_f32 v6, v54, v55 op_sel:[0,0,1]
	v_cvt_pk_fp8_f32 v7, v50, v51 op_sel:[0,0,1]
	v_lshl_add_u32 v3, v2, 11, v16
	global_store_dwordx4 v3, v[4:7], s[18:19]
	s_nop 1
	v_cvt_pk_fp8_f32 v2, v44, v45
	v_cvt_pk_fp8_f32 v3, v40, v41
	v_cvt_pk_fp8_f32 v4, v36, v37
	v_cvt_pk_fp8_f32 v5, v32, v33
	s_waitcnt lgkmcnt(0)
	v_cvt_pk_fp8_f32 v2, v46, v47 op_sel:[0,0,1]
	v_cvt_pk_fp8_f32 v3, v42, v43 op_sel:[0,0,1]
	v_cvt_pk_fp8_f32 v4, v38, v39 op_sel:[0,0,1]
	v_cvt_pk_fp8_f32 v5, v34, v35 op_sel:[0,0,1]
	s_and_b64 vcc, exec, s[4:5]
	s_mov_b64 s[4:5], -1
	v_lshl_add_u32 v1, v0, 11, v16
	global_store_dwordx4 v1, v[2:5], s[18:19]
	s_nop 1
	s_cbranch_vccnz .LBB0_838
	s_andn2_b64 vcc, exec, s[16:17]
	s_cbranch_vccnz .LBB0_837
	s_barrier
	s_branch .LBB0_837

; __device__ __forceinline__ unsigned pk4_fp8(float a, float b, float c, float d) { int r = __builtin_amdgcn_cvt_pk_fp8_f32(a, b, 0, false); r = __builtin_amdgcn_cvt_pk_fp8_f32(c, d, r, true); return (unsigned)r; }
;     __device__ __forceinline__ void operator()(const f32x4 (&acc)[2][2][4][2], const Unit& u, int wr, int wc, int fr, int fq) const {
;         const int row0 = u.pm * BM + wr * 64 + fr, col0 = (u.pn & 3) * 128 + wc * 32 + 8 * fq;
; #pragma unroll
;         for (int ai = 0; ai < 2; ++ai)
; #pragma unroll
;             for (int m = 0; m < 4; ++m) { float r[8];
; #pragma unroll
;                 for (int n = 0; n < 2; ++n)
; #pragma unroll
;                     for (int e = 0; e < 4; ++e) { const float g = acc[ai][0][m][n][e], up = acc[ai][1][m][n][e]; r[4 * n + e] = g * __builtin_amdgcn_rcpf(1.0f + __builtin_amdgcn_exp2f(-g * LOG2E)) * up * (float)(1 << ASHIFT); }
;                 v2u w; w.x = pk4_fp8(r[0], r[1], r[2], r[3]); w.y = pk4_fp8(r[4], r[5], r[6], r[7]);
;                 *(v2u*)(O + (size_t)(row0 + ai * HALF + m * 16) * EH + col0) = w; }
;     }
.LBB0_1661:
	s_mov_b32 s98, 0xbfb8aa3b
	s_mov_b32 s100, 0x41800000
	s_nop 15
	s_nop 15
	v_lshl_add_u32 v4, s87, 8, v203
	s_lshl_b32 s6, s88, 7
	s_and_b32 s6, s6, 0x180
	v_ashrrev_i32_e32 v5, 31, v4
	v_add_u32_e32 v2, s6, v205
	v_lshlrev_b64 v[0:1], 9, v[4:5]
	v_ashrrev_i32_e32 v3, 31, v2
	v_lshl_add_u64 v[0:1], s[24:25], 0, v[0:1]
	v_lshl_add_u64 v[0:1], v[0:1], 0, v[2:3]
	v_pk_mul_f32 v[228:229], v[192:193], s[98:99] op_sel_hi:[1,0]
	v_pk_mul_f32 v[230:231], v[194:195], s[98:99] op_sel_hi:[1,0]
	v_pk_mul_f32 v[232:233], v[184:185], s[98:99] op_sel_hi:[1,0]
	v_pk_mul_f32 v[234:235], v[186:187], s[98:99] op_sel_hi:[1,0]
	v_exp_f32_e32 v228, v228
	v_exp_f32_e32 v229, v229
	v_exp_f32_e32 v230, v230
	v_exp_f32_e32 v231, v231
	v_exp_f32_e32 v232, v232
	v_exp_f32_e32 v233, v233
	v_exp_f32_e32 v234, v234
	v_exp_f32_e32 v235, v235
	v_pk_add_f32 v[228:229], v[228:229], 1.0 op_sel_hi:[1,0]
	v_pk_add_f32 v[230:231], v[230:231], 1.0 op_sel_hi:[1,0]
	v_pk_add_f32 v[232:233], v[232:233], 1.0 op_sel_hi:[1,0]
	v_pk_add_f32 v[234:235], v[234:235], 1.0 op_sel_hi:[1,0]
	v_rcp_f32_e32 v228, v228
	v_rcp_f32_e32 v229, v229
	v_rcp_f32_e32 v230, v230
	v_rcp_f32_e32 v231, v231
	v_rcp_f32_e32 v232, v232
	v_rcp_f32_e32 v233, v233
	v_rcp_f32_e32 v234, v234
	v_rcp_f32_e32 v235, v235
	v_pk_mul_f32 v[228:229], v[192:193], v[228:229]
	v_pk_mul_f32 v[230:231], v[194:195], v[230:231]
	v_pk_mul_f32 v[232:233], v[184:185], v[232:233]
	v_pk_mul_f32 v[234:235], v[186:187], v[234:235]
	v_pk_mul_f32 v[228:229], v[188:189], v[228:229]
	v_pk_mul_f32 v[230:231], v[190:191], v[230:231]
	v_pk_mul_f32 v[232:233], v[180:181], v[232:233]
	v_pk_mul_f32 v[234:235], v[182:183], v[234:235]
	v_pk_mul_f32 v[228:229], s[100:101], v[228:229] op_sel_hi:[0,1]
	v_pk_mul_f32 v[230:231], s[100:101], v[230:231] op_sel_hi:[0,1]
	v_pk_mul_f32 v[232:233], s[100:101], v[232:233] op_sel_hi:[0,1]
	v_pk_mul_f32 v[234:235], s[100:101], v[234:235] op_sel_hi:[0,1]
	v_cvt_pk_fp8_f32 v244, v228, v229
	v_cvt_pk_fp8_f32 v245, v232, v233
	v_cvt_pk_fp8_f32 v244, v230, v231 op_sel:[0,0,1]
	v_cvt_pk_fp8_f32 v245, v234, v235 op_sel:[0,0,1]
	s_nop 0
	global_store_dwordx2 v[0:1], v[244:245], off
	v_or_b32_e32 v8, 16, v4
	v_ashrrev_i32_e32 v9, 31, v8
	v_lshlrev_b64 v[8:9], 9, v[8:9]
	v_lshl_add_u64 v[8:9], s[24:25], 0, v[8:9]
	v_lshl_add_u64 v[8:9], v[8:9], 0, v[2:3]
	v_pk_mul_f32 v[228:229], v[176:177], s[98:99] op_sel_hi:[1,0]
	v_pk_mul_f32 v[230:231], v[178:179], s[98:99] op_sel_hi:[1,0]
	v_pk_mul_f32 v[232:233], v[168:169], s[98:99] op_sel_hi:[1,0]
	v_pk_mul_f32 v[234:235], v[170:171], s[98:99] op_sel_hi:[1,0]
	v_exp_f32_e32 v228, v228
	v_exp_f32_e32 v229, v229
	v_exp_f32_e32 v230, v230
	v_exp_f32_e32 v231, v231
	v_exp_f32_e32 v232, v232
	v_exp_f32_e32 v233, v233
	v_exp_f32_e32 v234, v234
	v_exp_f32_e32 v235, v235
	v_pk_add_f32 v[228:229], v[228:229], 1.0 op_sel_hi:[1,0]
	v_pk_add_f32 v[230:231], v[230:231], 1.0 op_sel_hi:[1,0]
	v_pk_add_f32 v[232:233], v[232:233], 1.0 op_sel_hi:[1,0]
	v_pk_add_f32 v[234:235], v[234:235], 1.0 op_sel_hi:[1,0]
	v_rcp_f32_e32 v228, v228
	v_rcp_f32_e32 v229, v229
	v_rcp_f32_e32 v230, v230
	v_rcp_f32_e32 v231, v231
	v_rcp_f32_e32 v232, v232
	v_rcp_f32_e32 v233, v233
	v_rcp_f32_e32 v234, v234
	v_rcp_f32_e32 v235, v235
	v_pk_mul_f32 v[228:229], v[176:177], v[228:229]
	v_pk_mul_f32 v[230:231], v[178:179], v[230:231]
	v_pk_mul_f32 v[232:233], v[168:169], v[232:233]
	v_pk_mul_f32 v[234:235], v[170:171], v[234:235]
	v_pk_mul_f32 v[228:229], v[172:173], v[228:229]
	v_pk_mul_f32 v[230:231], v[174:175], v[230:231]
	v_pk_mul_f32 v[232:233], v[164:165], v[232:233]
	v_pk_mul_f32 v[234:235], v[166:167], v[234:235]
	v_pk_mul_f32 v[228:229], s[100:101], v[228:229] op_sel_hi:[0,1]
	v_pk_mul_f32 v[230:231], s[100:101], v[230:231] op_sel_hi:[0,1]
	v_pk_mul_f32 v[232:233], s[100:101], v[232:233] op_sel_hi:[0,1]
	v_pk_mul_f32 v[234:235], s[100:101], v[234:235] op_sel_hi:[0,1]
	v_cvt_pk_fp8_f32 v244, v228, v229
	v_cvt_pk_fp8_f32 v245, v232, v233
	v_cvt_pk_fp8_f32 v244, v230, v231 op_sel:[0,0,1]
	v_cvt_pk_fp8_f32 v245, v234, v235 op_sel:[0,0,1]
	s_nop 0
	global_store_dwordx2 v[8:9], v[244:245], off
	v_or_b32_e32 v8, 32, v4
	v_ashrrev_i32_e32 v9, 31, v8
	v_lshlrev_b64 v[8:9], 9, v[8:9]
	v_lshl_add_u64 v[8:9], s[24:25], 0, v[8:9]
	v_lshl_add_u64 v[8:9], v[8:9], 0, v[2:3]
	v_pk_mul_f32 v[228:229], v[160:161], s[98:99] op_sel_hi:[1,0]
	v_pk_mul_f32 v[230:231], v[162:163], s[98:99] op_sel_hi:[1,0]
	v_pk_mul_f32 v[232:233], v[152:153], s[98:99] op_sel_hi:[1,0]
	v_pk_mul_f32 v[234:235], v[154:155], s[98:99] op_sel_hi:[1,0]
	v_exp_f32_e32 v228, v228
	v_exp_f32_e32 v229, v229
	v_exp_f32_e32 v230, v230
	v_exp_f32_e32 v231, v231
	v_exp_f32_e32 v232, v232
	v_exp_f32_e32 v233, v233
	v_exp_f32_e32 v234, v234
	v_exp_f32_e32 v235, v235
	v_pk_add_f32 v[228:229], v[228:229], 1.0 op_sel_hi:[1,0]
	v_pk_add_f32 v[230:231], v[230:231], 1.0 op_sel_hi:[1,0]
	v_pk_add_f32 v[232:233], v[232:233], 1.0 op_sel_hi:[1,0]
	v_pk_add_f32 v[234:235], v[234:235], 1.0 op_sel_hi:[1,0]
	v_rcp_f32_e32 v228, v228
	v_rcp_f32_e32 v229, v229
	v_rcp_f32_e32 v230, v230
	v_rcp_f32_e32 v231, v231
	v_rcp_f32_e32 v232, v232
	v_rcp_f32_e32 v233, v233
	v_rcp_f32_e32 v234, v234
	v_rcp_f32_e32 v235, v235
	v_pk_mul_f32 v[228:229], v[160:161], v[228:229]
	v_pk_mul_f32 v[230:231], v[162:163], v[230:231]
	v_pk_mul_f32 v[232:233], v[152:153], v[232:233]
	v_pk_mul_f32 v[234:235], v[154:155], v[234:235]
	v_pk_mul_f32 v[228:229], v[156:157], v[228:229]
	v_pk_mul_f32 v[230:231], v[158:159], v[230:231]
	v_pk_mul_f32 v[232:233], v[148:149], v[232:233]
	v_pk_mul_f32 v[234:235], v[150:151], v[234:235]
	v_pk_mul_f32 v[228:229], s[100:101], v[228:229] op_sel_hi:[0,1]
; __device__ __forceinline__ unsigned pk4_fp8(float a, float b, float c, float d) { int r = __builtin_amdgcn_cvt_pk_fp8_f32(a, b, 0, false); r = __builtin_amdgcn_cvt_pk_fp8_f32(c, d, r, true); return (unsigned)r; }
;     __device__ __forceinline__ void operator()(const f32x4 (&acc)[2][2][4][2], const Unit& u, int wr, int wc, int fr, int fq) const {
;         const int row0 = u.pm * BM + wr * 64 + fr, col0 = (u.pn & 3) * 128 + wc * 32 + 8 * fq;
; #pragma unroll
;         for (int ai = 0; ai < 2; ++ai)
; #pragma unroll
;             for (int m = 0; m < 4; ++m) { float r[8];
; #pragma unroll
;                 for (int n = 0; n < 2; ++n)
; #pragma unroll
;                     for (int e = 0; e < 4; ++e) { const float g = acc[ai][0][m][n][e], up = acc[ai][1][m][n][e]; r[4 * n + e] = g * __builtin_amdgcn_rcpf(1.0f + __builtin_amdgcn_exp2f(-g * LOG2E)) * up * (float)(1 << ASHIFT); }
;                 v2u w; w.x = pk4_fp8(r[0], r[1], r[2], r[3]); w.y = pk4_fp8(r[4], r[5], r[6], r[7]);
;                 *(v2u*)(O + (size_t)(row0 + ai * HALF + m * 16) * EH + col0) = w; }
;     }
	v_pk_mul_f32 v[230:231], s[100:101], v[230:231] op_sel_hi:[0,1]
	v_pk_mul_f32 v[232:233], s[100:101], v[232:233] op_sel_hi:[0,1]
	v_pk_mul_f32 v[234:235], s[100:101], v[234:235] op_sel_hi:[0,1]
	v_cvt_pk_fp8_f32 v244, v228, v229
	v_cvt_pk_fp8_f32 v245, v232, v233
	v_cvt_pk_fp8_f32 v244, v230, v231 op_sel:[0,0,1]
	v_cvt_pk_fp8_f32 v245, v234, v235 op_sel:[0,0,1]
	s_nop 0
	global_store_dwordx2 v[8:9], v[244:245], off
	v_or_b32_e32 v4, 48, v4
	v_ashrrev_i32_e32 v5, 31, v4
	v_lshlrev_b64 v[4:5], 9, v[4:5]
	v_lshl_add_u64 v[4:5], s[24:25], 0, v[4:5]
	v_lshl_add_u64 v[2:3], v[4:5], 0, v[2:3]
	v_pk_mul_f32 v[228:229], v[144:145], s[98:99] op_sel_hi:[1,0]
	v_pk_mul_f32 v[230:231], v[146:147], s[98:99] op_sel_hi:[1,0]
	v_pk_mul_f32 v[232:233], v[136:137], s[98:99] op_sel_hi:[1,0]
	v_pk_mul_f32 v[234:235], v[138:139], s[98:99] op_sel_hi:[1,0]
	v_exp_f32_e32 v228, v228
	v_exp_f32_e32 v229, v229
	v_exp_f32_e32 v230, v230
	v_exp_f32_e32 v231, v231
	v_exp_f32_e32 v232, v232
	v_exp_f32_e32 v233, v233
	v_exp_f32_e32 v234, v234
	v_exp_f32_e32 v235, v235
	v_pk_add_f32 v[228:229], v[228:229], 1.0 op_sel_hi:[1,0]
	v_pk_add_f32 v[230:231], v[230:231], 1.0 op_sel_hi:[1,0]
	v_pk_add_f32 v[232:233], v[232:233], 1.0 op_sel_hi:[1,0]
	v_pk_add_f32 v[234:235], v[234:235], 1.0 op_sel_hi:[1,0]
	v_rcp_f32_e32 v228, v228
	v_rcp_f32_e32 v229, v229
	v_rcp_f32_e32 v230, v230
	v_rcp_f32_e32 v231, v231
	v_rcp_f32_e32 v232, v232
	v_rcp_f32_e32 v233, v233
	v_rcp_f32_e32 v234, v234
	v_rcp_f32_e32 v235, v235
	v_pk_mul_f32 v[228:229], v[144:145], v[228:229]
	v_pk_mul_f32 v[230:231], v[146:147], v[230:231]
	v_pk_mul_f32 v[232:233], v[136:137], v[232:233]
	v_pk_mul_f32 v[234:235], v[138:139], v[234:235]
	v_pk_mul_f32 v[228:229], v[140:141], v[228:229]
	v_pk_mul_f32 v[230:231], v[142:143], v[230:231]
	v_pk_mul_f32 v[232:233], v[132:133], v[232:233]
	v_pk_mul_f32 v[234:235], v[134:135], v[234:235]
	v_pk_mul_f32 v[228:229], s[100:101], v[228:229] op_sel_hi:[0,1]
	v_pk_mul_f32 v[230:231], s[100:101], v[230:231] op_sel_hi:[0,1]
	v_pk_mul_f32 v[232:233], s[100:101], v[232:233] op_sel_hi:[0,1]
	v_pk_mul_f32 v[234:235], s[100:101], v[234:235] op_sel_hi:[0,1]
	v_cvt_pk_fp8_f32 v244, v228, v229
	v_cvt_pk_fp8_f32 v245, v232, v233
	v_cvt_pk_fp8_f32 v244, v230, v231 op_sel:[0,0,1]
	v_cvt_pk_fp8_f32 v245, v234, v235 op_sel:[0,0,1]
	s_nop 0
	global_store_dwordx2 v[2:3], v[244:245], off
	v_add_co_u32_e32 v4, vcc, s50, v0
	s_nop 0
	v_addc_co_u32_e32 v5, vcc, 0, v1, vcc
	v_pk_mul_f32 v[228:229], v[128:129], s[98:99] op_sel_hi:[1,0]
	v_pk_mul_f32 v[230:231], v[130:131], s[98:99] op_sel_hi:[1,0]
	v_pk_mul_f32 v[232:233], v[120:121], s[98:99] op_sel_hi:[1,0]
	v_pk_mul_f32 v[234:235], v[122:123], s[98:99] op_sel_hi:[1,0]
	v_exp_f32_e32 v228, v228
	v_exp_f32_e32 v229, v229
	v_exp_f32_e32 v230, v230
	v_exp_f32_e32 v231, v231
	v_exp_f32_e32 v232, v232
	v_exp_f32_e32 v233, v233
	v_exp_f32_e32 v234, v234
	v_exp_f32_e32 v235, v235
	v_pk_add_f32 v[228:229], v[228:229], 1.0 op_sel_hi:[1,0]
	v_pk_add_f32 v[230:231], v[230:231], 1.0 op_sel_hi:[1,0]
	v_pk_add_f32 v[232:233], v[232:233], 1.0 op_sel_hi:[1,0]
	v_pk_add_f32 v[234:235], v[234:235], 1.0 op_sel_hi:[1,0]
	v_rcp_f32_e32 v228, v228
	v_rcp_f32_e32 v229, v229
	v_rcp_f32_e32 v230, v230
	v_rcp_f32_e32 v231, v231
	v_rcp_f32_e32 v232, v232
	v_rcp_f32_e32 v233, v233
	v_rcp_f32_e32 v234, v234
	v_rcp_f32_e32 v235, v235
	v_pk_mul_f32 v[228:229], v[128:129], v[228:229]
	v_pk_mul_f32 v[230:231], v[130:131], v[230:231]
	v_pk_mul_f32 v[232:233], v[120:121], v[232:233]
	v_pk_mul_f32 v[234:235], v[122:123], v[234:235]
	v_pk_mul_f32 v[228:229], v[124:125], v[228:229]
	v_pk_mul_f32 v[230:231], v[126:127], v[230:231]
	v_pk_mul_f32 v[232:233], v[116:117], v[232:233]
	v_pk_mul_f32 v[234:235], v[118:119], v[234:235]
	v_pk_mul_f32 v[228:229], s[100:101], v[228:229] op_sel_hi:[0,1]
	v_pk_mul_f32 v[230:231], s[100:101], v[230:231] op_sel_hi:[0,1]
	v_pk_mul_f32 v[232:233], s[100:101], v[232:233] op_sel_hi:[0,1]
	v_pk_mul_f32 v[234:235], s[100:101], v[234:235] op_sel_hi:[0,1]
	v_cvt_pk_fp8_f32 v244, v228, v229
	v_cvt_pk_fp8_f32 v245, v232, v233
	v_cvt_pk_fp8_f32 v244, v230, v231 op_sel:[0,0,1]
	v_cvt_pk_fp8_f32 v245, v234, v235 op_sel:[0,0,1]
	s_nop 0
	global_store_dwordx2 v[4:5], v[244:245], off
	v_add_co_u32_e32 v4, vcc, s52, v0
	s_nop 0
	v_addc_co_u32_e32 v5, vcc, 0, v1, vcc
	v_pk_mul_f32 v[228:229], v[112:113], s[98:99] op_sel_hi:[1,0]
	v_pk_mul_f32 v[230:231], v[114:115], s[98:99] op_sel_hi:[1,0]
	v_pk_mul_f32 v[232:233], v[104:105], s[98:99] op_sel_hi:[1,0]
	v_pk_mul_f32 v[234:235], v[106:107], s[98:99] op_sel_hi:[1,0]
	v_exp_f32_e32 v228, v228
	v_exp_f32_e32 v229, v229
	v_exp_f32_e32 v230, v230
	v_exp_f32_e32 v231, v231
	v_exp_f32_e32 v232, v232
	v_exp_f32_e32 v233, v233
	v_exp_f32_e32 v234, v234
	v_exp_f32_e32 v235, v235
	v_pk_add_f32 v[228:229], v[228:229], 1.0 op_sel_hi:[1,0]
	v_pk_add_f32 v[230:231], v[230:231], 1.0 op_sel_hi:[1,0]
	v_pk_add_f32 v[232:233], v[232:233], 1.0 op_sel_hi:[1,0]
; __device__ __forceinline__ unsigned pk4_fp8(float a, float b, float c, float d) { int r = __builtin_amdgcn_cvt_pk_fp8_f32(a, b, 0, false); r = __builtin_amdgcn_cvt_pk_fp8_f32(c, d, r, true); return (unsigned)r; }
;     __device__ __forceinline__ void operator()(const f32x4 (&acc)[2][2][4][2], const Unit& u, int wr, int wc, int fr, int fq) const {
;         const int row0 = u.pm * BM + wr * 64 + fr, col0 = (u.pn & 3) * 128 + wc * 32 + 8 * fq;
; #pragma unroll
;         for (int ai = 0; ai < 2; ++ai)
; #pragma unroll
;             for (int m = 0; m < 4; ++m) { float r[8];
; #pragma unroll
;                 for (int n = 0; n < 2; ++n)
; #pragma unroll
;                     for (int e = 0; e < 4; ++e) { const float g = acc[ai][0][m][n][e], up = acc[ai][1][m][n][e]; r[4 * n + e] = g * __builtin_amdgcn_rcpf(1.0f + __builtin_amdgcn_exp2f(-g * LOG2E)) * up * (float)(1 << ASHIFT); }
;                 v2u w; w.x = pk4_fp8(r[0], r[1], r[2], r[3]); w.y = pk4_fp8(r[4], r[5], r[6], r[7]);
;                 *(v2u*)(O + (size_t)(row0 + ai * HALF + m * 16) * EH + col0) = w; }
;     }
	v_pk_add_f32 v[234:235], v[234:235], 1.0 op_sel_hi:[1,0]
	v_rcp_f32_e32 v228, v228
	v_rcp_f32_e32 v229, v229
	v_rcp_f32_e32 v230, v230
	v_rcp_f32_e32 v231, v231
	v_rcp_f32_e32 v232, v232
	v_rcp_f32_e32 v233, v233
	v_rcp_f32_e32 v234, v234
	v_rcp_f32_e32 v235, v235
	v_pk_mul_f32 v[228:229], v[112:113], v[228:229]
	v_pk_mul_f32 v[230:231], v[114:115], v[230:231]
	v_pk_mul_f32 v[232:233], v[104:105], v[232:233]
	v_pk_mul_f32 v[234:235], v[106:107], v[234:235]
	v_pk_mul_f32 v[228:229], v[108:109], v[228:229]
	v_pk_mul_f32 v[230:231], v[110:111], v[230:231]
	v_pk_mul_f32 v[232:233], v[100:101], v[232:233]
	v_pk_mul_f32 v[234:235], v[102:103], v[234:235]
	v_pk_mul_f32 v[228:229], s[100:101], v[228:229] op_sel_hi:[0,1]
	v_pk_mul_f32 v[230:231], s[100:101], v[230:231] op_sel_hi:[0,1]
	v_pk_mul_f32 v[232:233], s[100:101], v[232:233] op_sel_hi:[0,1]
	v_pk_mul_f32 v[234:235], s[100:101], v[234:235] op_sel_hi:[0,1]
	v_cvt_pk_fp8_f32 v244, v228, v229
	v_cvt_pk_fp8_f32 v245, v232, v233
	v_cvt_pk_fp8_f32 v244, v230, v231 op_sel:[0,0,1]
	v_cvt_pk_fp8_f32 v245, v234, v235 op_sel:[0,0,1]
	s_nop 0
	global_store_dwordx2 v[4:5], v[244:245], off
	v_add_co_u32_e32 v4, vcc, s54, v0
	s_nop 0
	v_addc_co_u32_e32 v5, vcc, 0, v1, vcc
	v_pk_mul_f32 v[228:229], v[96:97], s[98:99] op_sel_hi:[1,0]
	v_pk_mul_f32 v[230:231], v[98:99], s[98:99] op_sel_hi:[1,0]
	v_pk_mul_f32 v[232:233], v[88:89], s[98:99] op_sel_hi:[1,0]
	v_pk_mul_f32 v[234:235], v[90:91], s[98:99] op_sel_hi:[1,0]
	v_exp_f32_e32 v228, v228
	v_exp_f32_e32 v229, v229
	v_exp_f32_e32 v230, v230
	v_exp_f32_e32 v231, v231
	v_exp_f32_e32 v232, v232
	v_exp_f32_e32 v233, v233
	v_exp_f32_e32 v234, v234
	v_exp_f32_e32 v235, v235
	v_pk_add_f32 v[228:229], v[228:229], 1.0 op_sel_hi:[1,0]
	v_pk_add_f32 v[230:231], v[230:231], 1.0 op_sel_hi:[1,0]
	v_pk_add_f32 v[232:233], v[232:233], 1.0 op_sel_hi:[1,0]
	v_pk_add_f32 v[234:235], v[234:235], 1.0 op_sel_hi:[1,0]
	v_rcp_f32_e32 v228, v228
	v_rcp_f32_e32 v229, v229
	v_rcp_f32_e32 v230, v230
	v_rcp_f32_e32 v231, v231
	v_rcp_f32_e32 v232, v232
	v_rcp_f32_e32 v233, v233
	v_rcp_f32_e32 v234, v234
	v_rcp_f32_e32 v235, v235
	v_pk_mul_f32 v[228:229], v[96:97], v[228:229]
	v_pk_mul_f32 v[230:231], v[98:99], v[230:231]
	v_pk_mul_f32 v[232:233], v[88:89], v[232:233]
	v_pk_mul_f32 v[234:235], v[90:91], v[234:235]
	v_pk_mul_f32 v[228:229], v[92:93], v[228:229]
	v_pk_mul_f32 v[230:231], v[94:95], v[230:231]
	v_pk_mul_f32 v[232:233], v[84:85], v[232:233]
	v_pk_mul_f32 v[234:235], v[86:87], v[234:235]
	v_pk_mul_f32 v[228:229], s[100:101], v[228:229] op_sel_hi:[0,1]
	v_pk_mul_f32 v[230:231], s[100:101], v[230:231] op_sel_hi:[0,1]
	v_pk_mul_f32 v[232:233], s[100:101], v[232:233] op_sel_hi:[0,1]
	v_pk_mul_f32 v[234:235], s[100:101], v[234:235] op_sel_hi:[0,1]
	v_cvt_pk_fp8_f32 v244, v228, v229
	v_cvt_pk_fp8_f32 v245, v232, v233
	v_cvt_pk_fp8_f32 v244, v230, v231 op_sel:[0,0,1]
	v_cvt_pk_fp8_f32 v245, v234, v235 op_sel:[0,0,1]
	s_nop 0
	global_store_dwordx2 v[4:5], v[244:245], off
	v_add_co_u32_e32 v0, vcc, 0x16000, v0
	s_nop 1
	v_addc_co_u32_e32 v1, vcc, 0, v1, vcc
	s_and_b64 vcc, exec, s[4:5]
	s_mov_b64 s[4:5], -1
	v_pk_mul_f32 v[228:229], v[80:81], s[98:99] op_sel_hi:[1,0]
	v_pk_mul_f32 v[230:231], v[82:83], s[98:99] op_sel_hi:[1,0]
	v_pk_mul_f32 v[232:233], v[72:73], s[98:99] op_sel_hi:[1,0]
	v_pk_mul_f32 v[234:235], v[74:75], s[98:99] op_sel_hi:[1,0]
	v_exp_f32_e32 v228, v228
	v_exp_f32_e32 v229, v229
	v_exp_f32_e32 v230, v230
	v_exp_f32_e32 v231, v231
	v_exp_f32_e32 v232, v232
	v_exp_f32_e32 v233, v233
	v_exp_f32_e32 v234, v234
	v_exp_f32_e32 v235, v235
	v_pk_add_f32 v[228:229], v[228:229], 1.0 op_sel_hi:[1,0]
	v_pk_add_f32 v[230:231], v[230:231], 1.0 op_sel_hi:[1,0]
	v_pk_add_f32 v[232:233], v[232:233], 1.0 op_sel_hi:[1,0]
	v_pk_add_f32 v[234:235], v[234:235], 1.0 op_sel_hi:[1,0]
	v_rcp_f32_e32 v228, v228
	v_rcp_f32_e32 v229, v229
	v_rcp_f32_e32 v230, v230
	v_rcp_f32_e32 v231, v231
	v_rcp_f32_e32 v232, v232
	v_rcp_f32_e32 v233, v233
	v_rcp_f32_e32 v234, v234
	v_rcp_f32_e32 v235, v235
	v_pk_mul_f32 v[228:229], v[80:81], v[228:229]
	v_pk_mul_f32 v[230:231], v[82:83], v[230:231]
	v_pk_mul_f32 v[232:233], v[72:73], v[232:233]
	v_pk_mul_f32 v[234:235], v[74:75], v[234:235]
	v_pk_mul_f32 v[228:229], v[76:77], v[228:229]
	v_pk_mul_f32 v[230:231], v[78:79], v[230:231]
	v_pk_mul_f32 v[232:233], v[68:69], v[232:233]
	v_pk_mul_f32 v[234:235], v[70:71], v[234:235]
	v_pk_mul_f32 v[228:229], s[100:101], v[228:229] op_sel_hi:[0,1]
	v_pk_mul_f32 v[230:231], s[100:101], v[230:231] op_sel_hi:[0,1]
	v_pk_mul_f32 v[232:233], s[100:101], v[232:233] op_sel_hi:[0,1]
	v_pk_mul_f32 v[234:235], s[100:101], v[234:235] op_sel_hi:[0,1]
	v_cvt_pk_fp8_f32 v244, v228, v229
	v_cvt_pk_fp8_f32 v245, v232, v233
	v_cvt_pk_fp8_f32 v244, v230, v231 op_sel:[0,0,1]
	v_cvt_pk_fp8_f32 v245, v234, v235 op_sel:[0,0,1]
	s_nop 0
	global_store_dwordx2 v[0:1], v[244:245], off
	s_cbranch_vccnz .LBB0_1625
	s_andn2_b64 vcc, exec, s[22:23]
	s_cbranch_vccnz .LBB0_1624
	s_barrier
	s_branch .LBB0_1624
